# K2 loader tail: counted-wait ladder (each row converts as soon as its two loads land) instead of vmcnt(0) before the whole convert
# baseline (speedup 1.0000x reference)
.LBB1_11:
	s_and_b32 s0, s8, 0x380
	s_lshl_b32 s2, s0, 2
	s_add_u32 s0, s4, s2
	s_addc_u32 s1, s5, 0
	s_add_u32 s2, s6, s2
	s_addc_u32 s3, s7, 0
	global_load_dwordx4 v[64:67], v128, s[0:1] nt
	s_add_u32 s10, s0, 0x10000
	global_load_dwordx4 v[68:71], v128, s[2:3] nt
	s_addc_u32 s11, s1, 0
	global_load_dwordx4 v[72:75], v128, s[10:11] nt
	s_add_u32 s10, s2, 0x10000
	s_addc_u32 s11, s3, 0
	global_load_dwordx4 v[76:79], v128, s[10:11] nt
	s_add_u32 s10, s0, 0x20000
	s_addc_u32 s11, s1, 0
	global_load_dwordx4 v[80:83], v128, s[10:11] nt
	s_add_u32 s10, s2, 0x20000
	s_addc_u32 s11, s3, 0
	global_load_dwordx4 v[84:87], v128, s[10:11] nt
	s_add_u32 s10, s0, 0x30000
	s_addc_u32 s11, s1, 0
	global_load_dwordx4 v[88:91], v128, s[10:11] nt
	s_add_u32 s10, s2, 0x30000
	s_addc_u32 s11, s3, 0
	global_load_dwordx4 v[92:95], v128, s[10:11] nt
	s_add_u32 s10, s0, 0x40000
	s_addc_u32 s11, s1, 0
	global_load_dwordx4 v[96:99], v128, s[10:11] nt
	s_add_u32 s10, s2, 0x40000
	s_addc_u32 s11, s3, 0
	global_load_dwordx4 v[100:103], v128, s[10:11] nt
	s_add_u32 s10, s0, 0x50000
	s_addc_u32 s11, s1, 0
	global_load_dwordx4 v[104:107], v128, s[10:11] nt
	s_add_u32 s10, s2, 0x50000
	s_addc_u32 s11, s3, 0
	global_load_dwordx4 v[108:111], v128, s[10:11] nt
	s_add_u32 s10, s0, 0x60000
	s_addc_u32 s11, s1, 0
	global_load_dwordx4 v[112:115], v128, s[10:11] nt
	s_add_u32 s10, s2, 0x60000
	s_addc_u32 s11, s3, 0
	s_add_u32 s0, s0, 0x70000
	global_load_dwordx4 v[116:119], v128, s[10:11] nt
	s_addc_u32 s1, s1, 0
	global_load_dwordx4 v[120:123], v128, s[0:1] nt
	s_add_u32 s0, s2, 0x70000
	s_addc_u32 s1, s3, 0
	s_add_i32 s2, s8, 64
	global_load_dwordx4 v[124:127], v128, s[0:1] nt
	s_and_b32 s0, s2, 0x3c0
	s_lshl_b32 s0, s0, 2
	s_add_u32 s2, s4, s0
	s_addc_u32 s3, s5, 0
	s_waitcnt vmcnt(16)
	s_add_u32 s0, s6, s0
	v_pk_add_f32 v[2:3], v[2:3], v[6:7]
	v_pk_add_f32 v[0:1], v[0:1], v[4:5]
	v_pk_add_f32 v[4:5], v[10:11], v[14:15]
	v_pk_add_f32 v[6:7], v[8:9], v[12:13]
	s_addc_u32 s1, s7, 0
	v_add_u32_e32 v131, 0x24000, v129
	v_pk_add_f32 v[8:9], v[18:19], v[22:23]
	v_pk_add_f32 v[10:11], v[16:17], v[20:21]
	v_pk_add_f32 v[12:13], v[26:27], v[30:31]
	v_pk_add_f32 v[14:15], v[24:25], v[28:29]
	v_pk_add_f32 v[16:17], v[34:35], v[38:39]
	v_pk_add_f32 v[18:19], v[32:33], v[36:37]
	v_pk_add_f32 v[20:21], v[42:43], v[46:47]
	v_pk_add_f32 v[22:23], v[40:41], v[44:45]
	v_pk_add_f32 v[24:25], v[50:51], v[54:55]
	v_pk_add_f32 v[26:27], v[48:49], v[52:53]
	v_pk_add_f32 v[28:29], v[58:59], v[62:63]
	v_pk_add_f32 v[30:31], v[56:57], v[60:61]
	v_cvt_pk_f16_f32 v3, v2, v3
	v_cvt_pk_f16_f32 v2, v0, v1
	v_cvt_pk_f16_f32 v1, v4, v5
	v_cvt_pk_f16_f32 v0, v6, v7
	s_add_u32 s10, s2, 0x10000
	v_cvt_pk_f16_f32 v5, v8, v9
	v_cvt_pk_f16_f32 v4, v10, v11
	v_cvt_pk_f16_f32 v7, v12, v13
	v_cvt_pk_f16_f32 v6, v14, v15
	v_cvt_pk_f16_f32 v9, v16, v17
	v_cvt_pk_f16_f32 v8, v18, v19
	v_cvt_pk_f16_f32 v11, v20, v21
	v_cvt_pk_f16_f32 v10, v22, v23
	v_cvt_pk_f16_f32 v13, v24, v25
	v_cvt_pk_f16_f32 v12, v26, v27
	v_cvt_pk_f16_f32 v15, v28, v29
	v_cvt_pk_f16_f32 v14, v30, v31
	ds_write2st64_b64 v131, v[2:3], v[0:1] offset1:4
	ds_write2st64_b64 v131, v[4:5], v[6:7] offset0:8 offset1:12
	ds_write2st64_b64 v131, v[8:9], v[10:11] offset0:16 offset1:20
	ds_write2st64_b64 v131, v[12:13], v[14:15] offset0:24 offset1:28
	s_addc_u32 s11, s3, 0
	s_waitcnt lgkmcnt(0)
	s_barrier
	s_add_u32 s12, s0, 0x10000
	global_load_dwordx4 v[0:3], v128, s[2:3] nt
	s_addc_u32 s13, s1, 0
	global_load_dwordx4 v[4:7], v128, s[0:1] nt
	s_add_u32 s14, s2, 0x20000
	global_load_dwordx4 v[8:11], v128, s[10:11] nt
	s_addc_u32 s15, s3, 0
	global_load_dwordx4 v[12:15], v128, s[12:13] nt
	s_add_u32 s10, s0, 0x20000
	global_load_dwordx4 v[16:19], v128, s[14:15] nt
	s_addc_u32 s11, s1, 0
	global_load_dwordx4 v[20:23], v128, s[10:11] nt
	s_add_u32 s10, s2, 0x30000
	s_addc_u32 s11, s3, 0
	global_load_dwordx4 v[24:27], v128, s[10:11] nt
	s_add_u32 s10, s0, 0x30000
	s_addc_u32 s11, s1, 0
	global_load_dwordx4 v[28:31], v128, s[10:11] nt
	s_add_u32 s10, s2, 0x40000
	s_addc_u32 s11, s3, 0
	global_load_dwordx4 v[32:35], v128, s[10:11] nt
	s_add_u32 s10, s0, 0x40000
	s_addc_u32 s11, s1, 0
	global_load_dwordx4 v[36:39], v128, s[10:11] nt
	s_add_u32 s10, s2, 0x50000
	s_addc_u32 s11, s3, 0
	global_load_dwordx4 v[40:43], v128, s[10:11] nt
	s_add_u32 s10, s0, 0x50000
	s_addc_u32 s11, s1, 0
	global_load_dwordx4 v[44:47], v128, s[10:11] nt
	s_add_u32 s10, s2, 0x60000
	s_addc_u32 s11, s3, 0
	global_load_dwordx4 v[48:51], v128, s[10:11] nt
	s_add_u32 s10, s0, 0x60000
	s_addc_u32 s11, s1, 0
	s_add_u32 s2, s2, 0x70000
	global_load_dwordx4 v[52:55], v128, s[10:11] nt
	s_addc_u32 s3, s3, 0
	global_load_dwordx4 v[56:59], v128, s[2:3] nt
	s_add_u32 s0, s0, 0x70000
	s_addc_u32 s1, s1, 0
	global_load_dwordx4 v[60:63], v128, s[0:1] nt
	s_waitcnt vmcnt(16)
	s_add_i32 s9, s9, 2
	v_pk_add_f32 v[66:67], v[66:67], v[70:71]
	v_pk_add_f32 v[64:65], v[64:65], v[68:69]
	v_pk_add_f32 v[68:69], v[74:75], v[78:79]
	v_pk_add_f32 v[70:71], v[72:73], v[76:77]
	v_pk_add_f32 v[72:73], v[82:83], v[86:87]
	v_pk_add_f32 v[74:75], v[80:81], v[84:85]
	v_pk_add_f32 v[76:77], v[90:91], v[94:95]
	v_pk_add_f32 v[78:79], v[88:89], v[92:93]
	v_pk_add_f32 v[80:81], v[98:99], v[102:103]
	v_pk_add_f32 v[82:83], v[96:97], v[100:101]
	v_pk_add_f32 v[84:85], v[106:107], v[110:111]
	v_pk_add_f32 v[86:87], v[104:105], v[108:109]
	v_pk_add_f32 v[88:89], v[114:115], v[118:119]
	v_pk_add_f32 v[90:91], v[112:113], v[116:117]
	v_pk_add_f32 v[92:93], v[122:123], v[126:127]
	v_pk_add_f32 v[94:95], v[120:121], v[124:125]
	v_cvt_pk_f16_f32 v67, v66, v67
	v_cvt_pk_f16_f32 v66, v64, v65
	v_cvt_pk_f16_f32 v65, v68, v69
	v_cvt_pk_f16_f32 v64, v70, v71
	v_cvt_pk_f16_f32 v69, v72, v73
	v_cvt_pk_f16_f32 v68, v74, v75
	v_cvt_pk_f16_f32 v71, v76, v77
	v_cvt_pk_f16_f32 v70, v78, v79
	v_cvt_pk_f16_f32 v73, v80, v81
	v_cvt_pk_f16_f32 v72, v82, v83
	v_cvt_pk_f16_f32 v75, v84, v85
	v_cvt_pk_f16_f32 v74, v86, v87
	v_cvt_pk_f16_f32 v77, v88, v89
	v_cvt_pk_f16_f32 v76, v90, v91
	v_cvt_pk_f16_f32 v79, v92, v93
	v_cvt_pk_f16_f32 v78, v94, v95
	ds_write2st64_b64 v130, v[66:67], v[64:65] offset1:4
	ds_write2st64_b64 v130, v[68:69], v[70:71] offset0:8 offset1:12
	ds_write2st64_b64 v130, v[72:73], v[74:75] offset0:16 offset1:20
	ds_write2st64_b64 v130, v[76:77], v[78:79] offset0:24 offset1:28
	s_waitcnt lgkmcnt(0)
	s_barrier
	s_addk_i32 s8, 0x80
	s_cmp_gt_u32 s9, 11
	s_cbranch_scc0 .LBB1_11
	s_waitcnt vmcnt(14)
	v_add_u32_e32 v64, 0x24000, v129
	v_pk_add_f32 v[2:3], v[2:3], v[6:7]
	v_pk_add_f32 v[0:1], v[0:1], v[4:5]
	v_cvt_pk_f16_f32 v3, v2, v3
	v_cvt_pk_f16_f32 v2, v0, v1
	s_waitcnt vmcnt(12)
	v_pk_add_f32 v[0:1], v[10:11], v[14:15]
	v_pk_add_f32 v[4:5], v[8:9], v[12:13]
	v_cvt_pk_f16_f32 v1, v0, v1
	v_cvt_pk_f16_f32 v0, v4, v5
	ds_write2st64_b64 v64, v[2:3], v[0:1] offset1:4
	s_waitcnt vmcnt(10)
	v_pk_add_f32 v[0:1], v[18:19], v[22:23]
	v_pk_add_f32 v[2:3], v[16:17], v[20:21]
	v_cvt_pk_f16_f32 v1, v0, v1
	v_cvt_pk_f16_f32 v0, v2, v3
	s_waitcnt vmcnt(8)
	v_pk_add_f32 v[2:3], v[26:27], v[30:31]
	v_pk_add_f32 v[4:5], v[24:25], v[28:29]
	v_cvt_pk_f16_f32 v3, v2, v3
	v_cvt_pk_f16_f32 v2, v4, v5
	ds_write2st64_b64 v64, v[0:1], v[2:3] offset0:8 offset1:12
	s_waitcnt vmcnt(6)
	v_pk_add_f32 v[0:1], v[34:35], v[38:39]
	v_pk_add_f32 v[2:3], v[32:33], v[36:37]
	v_cvt_pk_f16_f32 v1, v0, v1
	v_cvt_pk_f16_f32 v0, v2, v3
	s_waitcnt vmcnt(4)
	v_pk_add_f32 v[2:3], v[42:43], v[46:47]
	v_pk_add_f32 v[4:5], v[40:41], v[44:45]
	v_cvt_pk_f16_f32 v3, v2, v3
	v_cvt_pk_f16_f32 v2, v4, v5
	ds_write2st64_b64 v64, v[0:1], v[2:3] offset0:16 offset1:20
	s_waitcnt vmcnt(2)
	v_pk_add_f32 v[0:1], v[50:51], v[54:55]
	v_pk_add_f32 v[2:3], v[48:49], v[52:53]
	v_cvt_pk_f16_f32 v1, v0, v1
	v_cvt_pk_f16_f32 v0, v2, v3
	s_waitcnt vmcnt(0)
	v_pk_add_f32 v[2:3], v[58:59], v[62:63]
	v_pk_add_f32 v[4:5], v[56:57], v[60:61]
	v_cvt_pk_f16_f32 v3, v2, v3
	v_cvt_pk_f16_f32 v2, v4, v5
	ds_write2st64_b64 v64, v[0:1], v[2:3] offset0:24 offset1:28
	s_waitcnt lgkmcnt(0)
	s_barrier
	s_waitcnt lgkmcnt(0)
	s_barrier
	s_endpgm
